# differential units assigned statically too (units 255 - id and 511 - id: short ones for the workgroups with long MLA units); no device-atomic claims for the MLA, stick-breaking and differential queues
# speedup vs baseline: 1.0086x; 1.0039x over previous
; __device__ __forceinline__ int lane_id() { unsigned m = ~0u; asm volatile("" : "+s"(m)); return (int)__builtin_amdgcn_mbcnt_hi(m, __builtin_amdgcn_mbcnt_lo(m, 0u)); }
; __device__ __forceinline__ void claim_fire(unsigned* ctr, int tid, int* pend) { if (tid == 0) *pend = (int)__hip_atomic_fetch_add(ctr, 1u, __ATOMIC_RELAXED, __HIP_MEMORY_SCOPE_AGENT); }
;     ...
;     const bf16_t* H = (const bf16_t*)(F.ws + WS_H); const float* slopes4 = (const float*)(F.ctl + CW_LAM) + 32;
;     const float lamv = ((const float*)(F.ctl + CW_LAM))[l]; const float* dgain = (const float*)(F.ctl + CW_LAM) + 64 + l * 64;
;     const unsigned kmv = __hip_atomic_load(F.ctl + CW_KMAX + l * 16 + (lane_id() & 15), __ATOMIC_RELAXED, __HIP_MEMORY_SCOPE_AGENT);
;     at::claim_fire(q1ctr, F.tid, &pend);
.LBB0_913:
	s_add_u32 s14, s52, 0x100
	s_addc_u32 s15, s53, 0
	s_ashr_i32 s73, s72, 31
	s_lshl_b64 s[2:3], s[72:73], 2
	s_add_u32 s2, s50, s2
	s_addc_u32 s3, s51, s3
	s_mov_b32 s1, -1
	global_load_dword v28, v182, s[2:3]
	s_lshl_b64 s[10:11], s[10:11], 2
	v_mbcnt_lo_u32_b32 v0, s1, 0
	v_mbcnt_hi_u32_b32 v0, s1, v0
	s_add_u32 s2, s50, s10
	v_and_b32_e32 v0, 15, v0
	v_writelane_b32 v255, s10, 7
	s_addc_u32 s3, s51, s11
	v_lshlrev_b32_e32 v0, 2, v0
	v_mov_b32_e32 v1, v31
	v_lshl_add_u64 v[0:1], s[2:3], 0, v[0:1]
	v_add_co_u32_e32 v0, vcc, 0x2000, v0
	v_writelane_b32 v255, s11, 8
	s_nop 0
	v_addc_co_u32_e32 v1, vcc, 0, v1, vcc
	global_load_dword v140, v[0:1], off offset:2048 sc1
	s_and_saveexec_b64 s[10:11], s[38:39]
	s_cbranch_execz .LBB0_917
	s_mov_b64 s[34:35], exec
	v_mbcnt_lo_u32_b32 v0, s34, 0
	v_mbcnt_hi_u32_b32 v0, s35, v0
	v_cmp_eq_u32_e32 vcc, 0, v0
	s_and_saveexec_b64 s[16:17], vcc
	s_cbranch_execz .LBB0_916
	s_sub_i32 s1, 0xff, s92
	v_mov_b32_e32 v1, s1
	s_nop 0

;     ...
;     if (nctr != nullptr && tid == 0) *pend = (int)__hip_atomic_fetch_add(nctr, 1u, __ATOMIC_RELAXED, __HIP_MEMORY_SCOPE_AGENT);
.LBB0_967:
	v_cmp_eq_u32_e32 vcc, 0, v106
	s_and_b64 s[42:43], s[16:17], vcc
	s_and_saveexec_b64 s[40:41], s[42:43]
	s_cbranch_execz .LBB0_971
	s_mov_b64 s[44:45], exec
	v_mbcnt_lo_u32_b32 v16, s44, 0
	v_mbcnt_hi_u32_b32 v16, s45, v16
	v_cmp_eq_u32_e32 vcc, 0, v16
	s_and_saveexec_b64 s[42:43], vcc
	s_cbranch_execz .LBB0_970
	s_bcnt1_i32_b64 s4, s[44:45]
	v_mov_b32_e32 v17, s4
	v_add_u32_e32 v192, 0x100, v192
